# hyena MFMA loop: the twelve 64-bit register-rotation moves written as 32-bit move pairs
# speedup vs baseline: 1.0041x; 1.0041x over previous
.LBB0_701:
	s_add_i32 s55, s55, 2
	s_min_u32 s10, s55, s64
	s_lshl_b32 s11, s10, 7
	s_waitcnt lgkmcnt(7)
	v_mfma_f32_32x32x16_bf16 v[18:33], v[138:141], v[170:173], v[18:33]
	v_subrev_u32_e32 v2, s11, v228
	v_subrev_u32_e32 v16, 64, v2
	v_subrev_u32_e32 v17, 56, v2
	ds_read_b64 v[178:179], v16
	v_subrev_u32_e32 v16, 32, v2
	s_add_i32 s10, s62, s10
	v_mfma_f32_32x32x16_bf16 v[50:65], v[4:7], v[170:173], v[50:65]
	ds_read_b64 v[180:181], v17
	v_subrev_u32_e32 v17, 24, v2
	s_waitcnt lgkmcnt(8)
	v_mfma_f32_32x32x16_bf16 v[18:33], v[12:15], v[166:169], v[18:33]
	ds_read_b64 v[170:171], v16
	v_add_u32_e32 v16, 8, v2
	v_mfma_f32_32x32x16_bf16 v[50:65], v[8:11], v[166:169], v[50:65]
	ds_read_b64 v[172:173], v17
	v_mov_b32_e32 v17, s54
	s_waitcnt lgkmcnt(9)
	v_mfma_f32_32x32x16_bf16 v[18:33], v[94:97], v[162:165], v[18:33]
	ds_read_b64 v[98:99], v2
	v_mfma_f32_32x32x16_bf16 v[50:65], v[138:141], v[162:165], v[50:65]
	ds_read_b64 v[100:101], v16
	v_add_u32_e32 v16, 40, v2
	s_waitcnt lgkmcnt(10)
	v_mfma_f32_32x32x16_bf16 v[18:33], v[90:93], v[158:161], v[18:33]
	ds_read_b64 v[102:103], v2 offset:32
	v_subrev_u32_e32 v2, s10, v226
	v_cmp_gt_u32_e32 vcc, 64, v2
	v_mul_lo_u32 v2, v2, s18
	v_mfma_f32_32x32x16_bf16 v[50:65], v[12:15], v[158:161], v[50:65]
	ds_read_b64 v[104:105], v16
	v_add_u32_e32 v16, s56, v2
	v_cndmask_b32_e32 v16, v17, v16, vcc
	v_add_u32_e32 v16, v16, v247
	v_add_u32_e32 v2, s57, v2
	v_cndmask_b32_e32 v2, v17, v2, vcc
	v_add_u32_e32 v2, v2, v247
	s_waitcnt lgkmcnt(11)
	v_mfma_f32_32x32x16_bf16 v[34:49], v[138:141], v[154:157], v[34:49]
	ds_read_b128 v[106:109], v16
	v_mfma_f32_32x32x16_bf16 v[66:81], v[4:7], v[154:157], v[66:81]
	ds_read_b128 v[110:113], v16 offset:32
	s_waitcnt lgkmcnt(12)
	v_mfma_f32_32x32x16_bf16 v[34:49], v[12:15], v[146:149], v[34:49]
	ds_read_b128 v[114:117], v16 offset:80
	v_mfma_f32_32x32x16_bf16 v[66:81], v[8:11], v[146:149], v[66:81]
	ds_read_b128 v[118:121], v16 offset:112
	v_mov_b32_e32 v148, v6
	v_mov_b32_e32 v149, v7
	v_mov_b32_e32 v146, v4
	v_mov_b32_e32 v147, v5
	s_waitcnt lgkmcnt(13)
	v_mfma_f32_32x32x16_bf16 v[34:49], v[94:97], v[142:145], v[34:49]
	ds_read_b128 v[122:125], v2
	s_waitcnt lgkmcnt(11)
	v_mov_b32_e32 v94, v178
	v_mov_b32_e32 v95, v179
	v_mov_b32_e32 v96, v180
	v_mov_b32_e32 v97, v181
	v_mfma_f32_32x32x16_bf16 v[66:81], v[138:141], v[142:145], v[66:81]
	ds_read_b128 v[126:129], v2 offset:32
	v_mov_b32_e32 v144, v10
	v_mov_b32_e32 v145, v11
	v_mov_b32_e32 v142, v8
	v_mov_b32_e32 v143, v9
	v_mfma_f32_32x32x16_bf16 v[34:49], v[90:93], v[150:153], v[34:49]
	ds_read_b128 v[130:133], v2 offset:80
	ds_read_b128 v[134:137], v2 offset:112
	s_waitcnt lgkmcnt(12)
	v_mov_b32_e32 v90, v170
	v_mov_b32_e32 v91, v171
	v_mov_b32_e32 v92, v172
	v_mov_b32_e32 v93, v173
	v_mfma_f32_32x32x16_bf16 v[66:81], v[12:15], v[150:153], v[66:81]
	s_cmp_ge_u32 s55, s63
	s_cbranch_scc1 .LBB0_706

.LBB0_704:
	s_andn2_b64 vcc, exec, s[10:11]
	s_cbranch_vccz .LBB0_701
	s_waitcnt lgkmcnt(1)
	v_mov_b32_e32 v144, v92
	v_mov_b32_e32 v145, v93
	v_mov_b32_e32 v148, v96
	v_mov_b32_e32 v149, v97
	s_mov_b32 s55, s42
	v_mov_b32_e32 v142, v90
	v_mov_b32_e32 v143, v91
	v_mov_b32_e32 v146, v94
	v_mov_b32_e32 v147, v95
	s_cmp_ge_u32 s55, s63
	s_cbranch_scc0 .LBB0_702
